# attention fast path: exp / row-sum / pack VALU placed in the PV MFMA gaps
# baseline (speedup 1.0000x reference)
.Lattn_fast:
	ds_read_b128 v[110:113], v75 offset:8192
	ds_read_b128 v[114:117], v75 offset:10240
	ds_read_b128 v[118:121], v75 offset:12288
	ds_read_b128 v[122:125], v75 offset:14336
	v_exp_f32_e32 v34, v34
	v_exp_f32_e32 v1, v1
	v_exp_f32_e32 v36, v36
	v_exp_f32_e32 v35, v35
	v_exp_f32_e32 v38, v38
	v_exp_f32_e32 v37, v37
	v_exp_f32_e32 v40, v40
	v_exp_f32_e32 v39, v39
	v_add_f32_e32 v84, 0, v34
	v_cvt_pk_f16_f32 v50, v34, v1
	v_add_f32_e32 v84, v84, v1
	v_cvt_pk_f16_f32 v51, v36, v35
	v_add_f32_e32 v84, v84, v36
	v_cvt_pk_f16_f32 v52, v38, v37
	v_add_f32_e32 v84, v84, v35
	v_cvt_pk_f16_f32 v53, v40, v39
	ds_read_b128 v[58:61], v73 offset:8192
	ds_read_b128 v[62:65], v73 offset:10240
	v_add_f32_e32 v84, v84, v38
	v_add_f32_e32 v84, v84, v37
	s_waitcnt lgkmcnt(2)
	v_mfma_f32_16x16x32_f16 v[26:29], v[110:113], v[50:53], v[26:29]
	v_exp_f32_e32 v42, v42
	v_exp_f32_e32 v41, v41
	v_add_f32_e32 v84, v84, v40
	v_mfma_f32_16x16x32_f16 v[22:25], v[114:117], v[50:53], v[22:25]
	v_exp_f32_e32 v44, v44
	v_exp_f32_e32 v43, v43
	v_add_f32_e32 v84, v84, v39
	ds_read_b128 v[110:113], v73 offset:12288
	ds_read_b128 v[114:117], v73 offset:14336
	v_mfma_f32_16x16x32_f16 v[18:21], v[118:121], v[50:53], v[18:21]
	v_exp_f32_e32 v46, v46
	v_exp_f32_e32 v45, v45
	v_add_f32_e32 v84, v84, v42
	v_mfma_f32_16x16x32_f16 v[14:17], v[122:125], v[50:53], v[14:17]
	v_exp_f32_e32 v48, v48
	v_exp_f32_e32 v47, v47
	v_add_f32_e32 v84, v84, v41
	v_cvt_pk_f16_f32 v54, v42, v41
	v_add_f32_e32 v84, v84, v44
	v_cvt_pk_f16_f32 v55, v44, v43
	v_add_f32_e32 v84, v84, v43
	v_cvt_pk_f16_f32 v56, v46, v45
	v_add_f32_e32 v84, v84, v46
	v_cvt_pk_f16_f32 v57, v48, v47
	v_add_f32_e32 v84, v84, v45
	s_waitcnt lgkmcnt(0)
	v_mfma_f32_16x16x32_f16 v[26:29], v[58:61], v[54:57], v[26:29]
	v_add_f32_e32 v84, v84, v48
	v_mfma_f32_16x16x32_f16 v[22:25], v[62:65], v[54:57], v[22:25]
	v_add_f32_e32 v84, v84, v47
	v_mfma_f32_16x16x32_f16 v[18:21], v[110:113], v[54:57], v[18:21]
	v_add_f32_e32 v68, v68, v84
	v_mfma_f32_16x16x32_f16 v[14:17], v[114:117], v[54:57], v[14:17]
	s_branch .LBB2_29
